# v13 + e_raw GEMM epilogue rewritten by hand (lean sum-of-squares, in-place cvt, bpermute lane transpose, quad-contiguous stores)
# baseline (speedup 1.0000x reference)
.LBB0_445:
	s_barrier
	s_lshl_b32 s4, s0, 8
	s_mov_b32 s74, s96
	v_lshrrev_b32_e32 v160, 2, v248
	v_and_b32_e32 v161, 3, v248
	v_lshlrev_b32_e32 v158, 6, v161
	v_lshl_add_u32 v158, v160, 2, v158
	s_add_i32 s5, s4, s75
	v_add_u32_e32 v162, s5, v160
	s_lshl_b32 s1, s73, 5
	s_lshl_b32 s5, s8, 8
	s_or_b32 s1, s1, s5
	v_lshl_or_b32 v163, v161, 3, s1
	v_lshlrev_b32_e32 v162, 11, v162
	v_lshl_add_u32 v162, v163, 1, v162
	v_mov_b32_e32 v163, 0
	v_lshl_add_u64 v[162:163], s[62:63], 0, v[162:163]
	v_xor_b32_e32 v164, 16, v248
	v_lshlrev_b32_e32 v164, 2, v164
	v_xor_b32_e32 v165, 32, v248
	v_lshlrev_b32_e32 v165, 2, v165
	s_lshl_b32 s5, s73, 2
	v_lshl_add_u32 v166, v148, 4, s5
	s_mov_b32 s98, 0x8000
	s_mov_b32 s99, 0
	s_mov_b32 s100, 0x28000
	s_mov_b32 s101, 0
	v_mul_f32_e32 v170, v126, v126
	v_fmac_f32_e32 v170, v127, v127
	v_fmac_f32_e32 v170, v128, v128
	v_fmac_f32_e32 v170, v129, v129
	v_fmac_f32_e32 v170, v122, v122
	v_fmac_f32_e32 v170, v123, v123
	v_fmac_f32_e32 v170, v124, v124
	v_fmac_f32_e32 v170, v125, v125
	v_cvt_pk_bf16_f32 v126, v126, v127
	v_cvt_pk_bf16_f32 v127, v128, v129
	v_cvt_pk_bf16_f32 v128, v122, v123
	v_cvt_pk_bf16_f32 v129, v124, v125
	ds_bpermute_b32 v126, v158, v126
	ds_bpermute_b32 v127, v158, v127
	ds_bpermute_b32 v128, v158, v128
	ds_bpermute_b32 v129, v158, v129
	v_fmac_f32_e32 v170, v118, v118
	v_fmac_f32_e32 v170, v119, v119
	v_fmac_f32_e32 v170, v120, v120
	v_fmac_f32_e32 v170, v121, v121
	v_fmac_f32_e32 v170, v110, v110
	v_fmac_f32_e32 v170, v111, v111
	v_fmac_f32_e32 v170, v112, v112
	v_fmac_f32_e32 v170, v113, v113
	v_cvt_pk_bf16_f32 v118, v118, v119
	v_cvt_pk_bf16_f32 v119, v120, v121
	v_cvt_pk_bf16_f32 v120, v110, v111
	v_cvt_pk_bf16_f32 v121, v112, v113
	ds_bpermute_b32 v118, v158, v118
	ds_bpermute_b32 v119, v158, v119
	ds_bpermute_b32 v120, v158, v120
	ds_bpermute_b32 v121, v158, v121
	s_waitcnt lgkmcnt(4)
	global_store_dwordx4 v[162:163], v[126:129], off
	v_mul_f32_e32 v171, v114, v114
	v_fmac_f32_e32 v171, v115, v115
	v_fmac_f32_e32 v171, v116, v116
	v_fmac_f32_e32 v171, v117, v117
	v_fmac_f32_e32 v171, v106, v106
	v_fmac_f32_e32 v171, v107, v107
	v_fmac_f32_e32 v171, v108, v108
	v_fmac_f32_e32 v171, v109, v109
	v_cvt_pk_bf16_f32 v114, v114, v115
	v_cvt_pk_bf16_f32 v115, v116, v117
	v_cvt_pk_bf16_f32 v116, v106, v107
	v_cvt_pk_bf16_f32 v117, v108, v109
	ds_bpermute_b32 v114, v158, v114
	ds_bpermute_b32 v115, v158, v115
	ds_bpermute_b32 v116, v158, v116
	ds_bpermute_b32 v117, v158, v117
	s_waitcnt lgkmcnt(4)
	global_store_dwordx4 v[162:163], v[118:121], off offset:256
	v_lshl_add_u64 v[162:163], v[162:163], 0, s[98:99]
	v_fmac_f32_e32 v171, v98, v98
	v_fmac_f32_e32 v171, v99, v99
	v_fmac_f32_e32 v171, v100, v100
	v_fmac_f32_e32 v171, v101, v101
	v_fmac_f32_e32 v171, v94, v94
	v_fmac_f32_e32 v171, v95, v95
	v_fmac_f32_e32 v171, v96, v96
	v_fmac_f32_e32 v171, v97, v97
	v_cvt_pk_bf16_f32 v98, v98, v99
	v_cvt_pk_bf16_f32 v99, v100, v101
	v_cvt_pk_bf16_f32 v100, v94, v95
	v_cvt_pk_bf16_f32 v101, v96, v97
	ds_bpermute_b32 v98, v158, v98
	ds_bpermute_b32 v99, v158, v99
	ds_bpermute_b32 v100, v158, v100
	ds_bpermute_b32 v101, v158, v101
	s_waitcnt lgkmcnt(4)
	global_store_dwordx4 v[162:163], v[114:117], off
	v_mul_f32_e32 v172, v102, v102
	v_fmac_f32_e32 v172, v103, v103
	v_fmac_f32_e32 v172, v104, v104
	v_fmac_f32_e32 v172, v105, v105
	v_fmac_f32_e32 v172, v90, v90
	v_fmac_f32_e32 v172, v91, v91
	v_fmac_f32_e32 v172, v92, v92
	v_fmac_f32_e32 v172, v93, v93
	v_cvt_pk_bf16_f32 v102, v102, v103
	v_cvt_pk_bf16_f32 v103, v104, v105
	v_cvt_pk_bf16_f32 v104, v90, v91
	v_cvt_pk_bf16_f32 v105, v92, v93
	ds_bpermute_b32 v102, v158, v102
	ds_bpermute_b32 v103, v158, v103
	ds_bpermute_b32 v104, v158, v104
	ds_bpermute_b32 v105, v158, v105
	s_waitcnt lgkmcnt(4)
	global_store_dwordx4 v[162:163], v[98:101], off offset:256
	v_lshl_add_u64 v[162:163], v[162:163], 0, s[98:99]
	v_fmac_f32_e32 v172, v82, v82
	v_fmac_f32_e32 v172, v83, v83
	v_fmac_f32_e32 v172, v84, v84
	v_fmac_f32_e32 v172, v85, v85
	v_fmac_f32_e32 v172, v78, v78
	v_fmac_f32_e32 v172, v79, v79
	v_fmac_f32_e32 v172, v80, v80
	v_fmac_f32_e32 v172, v81, v81
	v_cvt_pk_bf16_f32 v82, v82, v83
	v_cvt_pk_bf16_f32 v83, v84, v85
	v_cvt_pk_bf16_f32 v84, v78, v79
	v_cvt_pk_bf16_f32 v85, v80, v81
	ds_bpermute_b32 v82, v158, v82
	ds_bpermute_b32 v83, v158, v83
	ds_bpermute_b32 v84, v158, v84
	ds_bpermute_b32 v85, v158, v85
	s_waitcnt lgkmcnt(4)
	global_store_dwordx4 v[162:163], v[102:105], off
	v_mul_f32_e32 v173, v86, v86
	v_fmac_f32_e32 v173, v87, v87
	v_fmac_f32_e32 v173, v88, v88
	v_fmac_f32_e32 v173, v89, v89
	v_fmac_f32_e32 v173, v74, v74
	v_fmac_f32_e32 v173, v75, v75
	v_fmac_f32_e32 v173, v76, v76
	v_fmac_f32_e32 v173, v77, v77
	v_cvt_pk_bf16_f32 v86, v86, v87
	v_cvt_pk_bf16_f32 v87, v88, v89
	v_cvt_pk_bf16_f32 v88, v74, v75
	v_cvt_pk_bf16_f32 v89, v76, v77
	ds_bpermute_b32 v86, v158, v86
	ds_bpermute_b32 v87, v158, v87
	ds_bpermute_b32 v88, v158, v88
	ds_bpermute_b32 v89, v158, v89
	s_waitcnt lgkmcnt(4)
	global_store_dwordx4 v[162:163], v[82:85], off offset:256
	v_lshl_add_u64 v[162:163], v[162:163], 0, s[98:99]
	v_fmac_f32_e32 v173, v70, v70
	v_fmac_f32_e32 v173, v71, v71
	v_fmac_f32_e32 v173, v72, v72
	v_fmac_f32_e32 v173, v73, v73
	v_fmac_f32_e32 v173, v66, v66
	v_fmac_f32_e32 v173, v67, v67
	v_fmac_f32_e32 v173, v68, v68
	v_fmac_f32_e32 v173, v69, v69
	v_cvt_pk_bf16_f32 v70, v70, v71
	v_cvt_pk_bf16_f32 v71, v72, v73
	v_cvt_pk_bf16_f32 v72, v66, v67
	v_cvt_pk_bf16_f32 v73, v68, v69
	ds_bpermute_b32 v70, v158, v70
	ds_bpermute_b32 v71, v158, v71
	ds_bpermute_b32 v72, v158, v72
	ds_bpermute_b32 v73, v158, v73
	s_waitcnt lgkmcnt(4)
	global_store_dwordx4 v[162:163], v[86:89], off
	v_mul_f32_e32 v174, v62, v62
	v_fmac_f32_e32 v174, v63, v63
	v_fmac_f32_e32 v174, v64, v64
	v_fmac_f32_e32 v174, v65, v65
	v_fmac_f32_e32 v174, v58, v58
	v_fmac_f32_e32 v174, v59, v59
	v_fmac_f32_e32 v174, v60, v60
	v_fmac_f32_e32 v174, v61, v61
	v_cvt_pk_bf16_f32 v62, v62, v63
	v_cvt_pk_bf16_f32 v63, v64, v65
	v_cvt_pk_bf16_f32 v64, v58, v59
	v_cvt_pk_bf16_f32 v65, v60, v61
	ds_bpermute_b32 v62, v158, v62
	ds_bpermute_b32 v63, v158, v63
	ds_bpermute_b32 v64, v158, v64
	ds_bpermute_b32 v65, v158, v65
	s_waitcnt lgkmcnt(4)
	global_store_dwordx4 v[162:163], v[70:73], off offset:256
	v_lshl_add_u64 v[162:163], v[162:163], 0, s[100:101]
	v_fmac_f32_e32 v174, v50, v50
	v_fmac_f32_e32 v174, v51, v51
	v_fmac_f32_e32 v174, v52, v52
	v_fmac_f32_e32 v174, v53, v53
	v_fmac_f32_e32 v174, v46, v46
	v_fmac_f32_e32 v174, v47, v47
	v_fmac_f32_e32 v174, v48, v48
	v_fmac_f32_e32 v174, v49, v49
	v_cvt_pk_bf16_f32 v50, v50, v51
	v_cvt_pk_bf16_f32 v51, v52, v53
	v_cvt_pk_bf16_f32 v52, v46, v47
	v_cvt_pk_bf16_f32 v53, v48, v49
	ds_bpermute_b32 v50, v158, v50
	ds_bpermute_b32 v51, v158, v51
	ds_bpermute_b32 v52, v158, v52
	ds_bpermute_b32 v53, v158, v53
	s_waitcnt lgkmcnt(4)
	global_store_dwordx4 v[162:163], v[62:65], off
	v_mul_f32_e32 v175, v54, v54
	v_fmac_f32_e32 v175, v55, v55
	v_fmac_f32_e32 v175, v56, v56
	v_fmac_f32_e32 v175, v57, v57
	v_fmac_f32_e32 v175, v42, v42
	v_fmac_f32_e32 v175, v43, v43
	v_fmac_f32_e32 v175, v44, v44
	v_fmac_f32_e32 v175, v45, v45
	v_cvt_pk_bf16_f32 v54, v54, v55
	v_cvt_pk_bf16_f32 v55, v56, v57
	v_cvt_pk_bf16_f32 v56, v42, v43
	v_cvt_pk_bf16_f32 v57, v44, v45
	ds_bpermute_b32 v54, v158, v54
	ds_bpermute_b32 v55, v158, v55
	ds_bpermute_b32 v56, v158, v56
	ds_bpermute_b32 v57, v158, v57
	s_waitcnt lgkmcnt(4)
	global_store_dwordx4 v[162:163], v[50:53], off offset:256
	v_lshl_add_u64 v[162:163], v[162:163], 0, s[98:99]
	v_fmac_f32_e32 v175, v34, v34
	v_fmac_f32_e32 v175, v35, v35
	v_fmac_f32_e32 v175, v36, v36
	v_fmac_f32_e32 v175, v37, v37
	v_fmac_f32_e32 v175, v30, v30
	v_fmac_f32_e32 v175, v31, v31
	v_fmac_f32_e32 v175, v32, v32
	v_fmac_f32_e32 v175, v33, v33
	v_cvt_pk_bf16_f32 v34, v34, v35
	v_cvt_pk_bf16_f32 v35, v36, v37
	v_cvt_pk_bf16_f32 v36, v30, v31
	v_cvt_pk_bf16_f32 v37, v32, v33
	ds_bpermute_b32 v34, v158, v34
	ds_bpermute_b32 v35, v158, v35
	ds_bpermute_b32 v36, v158, v36
	ds_bpermute_b32 v37, v158, v37
	s_waitcnt lgkmcnt(4)
	global_store_dwordx4 v[162:163], v[54:57], off
	v_mul_f32_e32 v176, v38, v38
	v_fmac_f32_e32 v176, v39, v39
	v_fmac_f32_e32 v176, v40, v40
	v_fmac_f32_e32 v176, v41, v41
	v_fmac_f32_e32 v176, v26, v26
	v_fmac_f32_e32 v176, v27, v27
	v_fmac_f32_e32 v176, v28, v28
	v_fmac_f32_e32 v176, v29, v29
	v_cvt_pk_bf16_f32 v38, v38, v39
	v_cvt_pk_bf16_f32 v39, v40, v41
	v_cvt_pk_bf16_f32 v40, v26, v27
	v_cvt_pk_bf16_f32 v41, v28, v29
	ds_bpermute_b32 v38, v158, v38
	ds_bpermute_b32 v39, v158, v39
	ds_bpermute_b32 v40, v158, v40
	ds_bpermute_b32 v41, v158, v41
	s_waitcnt lgkmcnt(4)
	global_store_dwordx4 v[162:163], v[34:37], off offset:256
	v_lshl_add_u64 v[162:163], v[162:163], 0, s[98:99]
	v_fmac_f32_e32 v176, v18, v18
	v_fmac_f32_e32 v176, v19, v19
	v_fmac_f32_e32 v176, v20, v20
	v_fmac_f32_e32 v176, v21, v21
	v_fmac_f32_e32 v176, v14, v14
	v_fmac_f32_e32 v176, v15, v15
	v_fmac_f32_e32 v176, v16, v16
	v_fmac_f32_e32 v176, v17, v17
	v_cvt_pk_bf16_f32 v18, v18, v19
	v_cvt_pk_bf16_f32 v19, v20, v21
	v_cvt_pk_bf16_f32 v20, v14, v15
	v_cvt_pk_bf16_f32 v21, v16, v17
	ds_bpermute_b32 v18, v158, v18
	ds_bpermute_b32 v19, v158, v19
	ds_bpermute_b32 v20, v158, v20
	ds_bpermute_b32 v21, v158, v21
	s_waitcnt lgkmcnt(4)
	global_store_dwordx4 v[162:163], v[38:41], off
	v_mul_f32_e32 v177, v22, v22
	v_fmac_f32_e32 v177, v23, v23
	v_fmac_f32_e32 v177, v24, v24
	v_fmac_f32_e32 v177, v25, v25
	v_fmac_f32_e32 v177, v10, v10
	v_fmac_f32_e32 v177, v11, v11
	v_fmac_f32_e32 v177, v12, v12
	v_fmac_f32_e32 v177, v13, v13
	v_cvt_pk_bf16_f32 v22, v22, v23
	v_cvt_pk_bf16_f32 v23, v24, v25
	v_cvt_pk_bf16_f32 v24, v10, v11
	v_cvt_pk_bf16_f32 v25, v12, v13
	ds_bpermute_b32 v22, v158, v22
	ds_bpermute_b32 v23, v158, v23
	ds_bpermute_b32 v24, v158, v24
	ds_bpermute_b32 v25, v158, v25
	s_waitcnt lgkmcnt(4)
	global_store_dwordx4 v[162:163], v[18:21], off offset:256
	v_lshl_add_u64 v[162:163], v[162:163], 0, s[98:99]
	v_fmac_f32_e32 v177, v6, v6
	v_fmac_f32_e32 v177, v7, v7
	v_fmac_f32_e32 v177, v8, v8
	v_fmac_f32_e32 v177, v9, v9
	v_fmac_f32_e32 v177, v2, v2
	v_fmac_f32_e32 v177, v3, v3
	v_fmac_f32_e32 v177, v4, v4
	v_fmac_f32_e32 v177, v5, v5
	v_cvt_pk_bf16_f32 v6, v6, v7
	v_cvt_pk_bf16_f32 v7, v8, v9
	v_cvt_pk_bf16_f32 v8, v2, v3
	v_cvt_pk_bf16_f32 v9, v4, v5
	ds_bpermute_b32 v6, v158, v6
	ds_bpermute_b32 v7, v158, v7
	ds_bpermute_b32 v8, v158, v8
	ds_bpermute_b32 v9, v158, v9
	s_waitcnt lgkmcnt(4)
	global_store_dwordx4 v[162:163], v[22:25], off
	s_waitcnt lgkmcnt(0)
	global_store_dwordx4 v[162:163], v[6:9], off offset:256
	ds_bpermute_b32 v178, v164, v170
	ds_bpermute_b32 v179, v164, v171
	ds_bpermute_b32 v180, v164, v172
	ds_bpermute_b32 v181, v164, v173
	ds_bpermute_b32 v182, v164, v174
	ds_bpermute_b32 v183, v164, v175
	ds_bpermute_b32 v184, v164, v176
	ds_bpermute_b32 v185, v164, v177
	s_waitcnt lgkmcnt(0)
	v_add_f32_e32 v170, v170, v178
	v_add_f32_e32 v171, v171, v179
	v_add_f32_e32 v172, v172, v180
	v_add_f32_e32 v173, v173, v181
	v_add_f32_e32 v174, v174, v182
	v_add_f32_e32 v175, v175, v183
	v_add_f32_e32 v176, v176, v184
	v_add_f32_e32 v177, v177, v185
	ds_bpermute_b32 v178, v165, v170
	ds_bpermute_b32 v179, v165, v171
	ds_bpermute_b32 v180, v165, v172
	ds_bpermute_b32 v181, v165, v173
	ds_bpermute_b32 v182, v165, v174
	ds_bpermute_b32 v183, v165, v175
	ds_bpermute_b32 v184, v165, v176
	ds_bpermute_b32 v185, v165, v177
	s_waitcnt lgkmcnt(0)
	v_add_f32_e32 v170, v170, v178
	v_add_f32_e32 v171, v171, v179
	v_add_f32_e32 v172, v172, v180
	v_add_f32_e32 v173, v173, v181
	v_add_f32_e32 v174, v174, v182
	v_add_f32_e32 v175, v175, v183
	v_add_f32_e32 v176, v176, v184
	v_add_f32_e32 v177, v177, v185
	v_cmp_gt_u32_e32 vcc, 16, v248
	s_and_saveexec_b64 s[0:1], vcc
	ds_write_b32 v166, v170
	ds_write_b32 v166, v171 offset:256
	ds_write_b32 v166, v172 offset:512
	ds_write_b32 v166, v173 offset:768
	ds_write_b32 v166, v174 offset:2048
	ds_write_b32 v166, v175 offset:2304
	ds_write_b32 v166, v176 offset:2560
	ds_write_b32 v166, v177 offset:2816
	s_or_b64 exec, exec, s[0:1]
	s_waitcnt lgkmcnt(0)
	s_barrier
	s_andn2_b32 s38, s38, 63
	v_or_b32_e32 v2, s38, v248
	s_movk_i32 s0, 0x100
	v_cmp_gt_i32_e32 vcc, s0, v2
	s_and_saveexec_b64 s[0:1], vcc
	s_cbranch_execz .LBB0_463
	v_lshl_add_u32 v3, v2, 4, 0
	s_waitcnt lgkmcnt(0)
	ds_read_b128 v[4:7], v3
	v_add_u32_e32 v2, s4, v2
	v_ashrrev_i32_e32 v3, 31, v2
	s_ashr_i32 s9, s8, 31
	v_lshl_add_u64 v[2:3], v[2:3], 4, s[46:47]
	s_waitcnt lgkmcnt(0)
	v_mov_b32_e32 v8, v5
	v_mov_b32_e32 v9, v6
	v_mov_b32_e32 v5, v7
	v_lshl_add_u64 v[2:3], s[8:9], 2, v[2:3]
	v_pk_add_f32 v[4:5], v[8:9], v[4:5]
	v_add_co_u32_e32 v2, vcc, 0x1df0000, v2
	v_add_f32_e32 v4, v4, v5
	s_nop 0
	v_addc_co_u32_e32 v3, vcc, 0, v3, vcc
	global_store_dword v[2:3], v4, off
